# RG-LRU carry step: 7 serialized branchy LDS-read+fma steps replaced by 7 up-front ds_read_b64 and a branch-free fmac+cndmask chain with counted lgkmcnt
# baseline (speedup 1.0000x reference)
; #define LAS __attribute__((address_space(3)))
; #define MFMA16(a, b, c) __builtin_amdgcn_mfma_f32_16x16x32_bf16((a), (b), (c), 0, 0, 0)
; __device__ __forceinline__ float fsig(float x) { return __builtin_amdgcn_rcpf(1.0f + __builtin_amdgcn_exp2f(-LOG2E * x)); }
; __device__ __forceinline__ void unit(LAS unsigned char* lds, const bf16* __restrict__ xr, const bf16* __restrict__ yg, const float* __restrict__ conv_w, const float* __restrict__ conv_b, const bf16* __restrict__ wga_t, const bf16* __restrict__ wgx_t, ...
;     ...
;         {
;             f32x4 ar[2] = {}, ai[2] = {};
; #pragma unroll
;             for (int ks = 0; ks < 4; ++ks) { const bf16x8 xfr = *(const LAS bf16x8*)(lds + XA_OFF + (16 * tb + l15) * XA_P + 64 * ks + 16 * l4);
; #pragma unroll
;                 for (int dt = 0; dt < 2; ++dt) { ar[dt] = MFMA16(wf[0][dt][ks], xfr, ar[dt]); ai[dt] = MFMA16(wf[1][dt][ks], xfr, ai[dt]); } }
;             const int tk = 16 * tb + l15;
; #pragma unroll
;             for (int dt = 0; dt < 2; ++dt) { const int dl = dq * 32 + 16 * dt + 4 * l4; const f32x4 xo = *(const LAS f32x4*)(XF + tk * 64 + dl); f32x4 av, bv;
; #pragma unroll
;                 for (int r = 0; r < 4; ++r) { const float rg = fsig(ar[dt][r] + cba[dt][r]), ig = fsig(ai[dt][r] + cbx[dt][r]); const float la = rg * csp[dt][r];
;                     const float a_ = __builtin_amdgcn_exp2f(LOG2E * la); av[r] = a_;
;                     bv[r] = __builtin_amdgcn_sqrtf(fmaxf(1.0f - a_ * a_, 0.f)) * (ig * xo[r]); }
;                 *(LAS f32x4*)(SA + tk * 68 + dl) = av; *(LAS f32x4*)(SB + tk * 68 + dl) = bv; }
;         }
;         asm volatile("s_waitcnt lgkmcnt(0)" ::: "memory"); __builtin_amdgcn_s_barrier(); asm volatile("" ::: "memory");
.LBB5_955:
	s_waitcnt lgkmcnt(0)
	s_barrier
	ds_read_b128 v[82:85], v161
	ds_read_b128 v[178:181], v161 offset:64
	s_and_b64 vcc, exec, s[4:5]
	s_waitcnt lgkmcnt(1)
	v_mfma_f32_16x16x32_bf16 v[86:89], v[2:5], v[82:85], 0
	v_mfma_f32_16x16x32_bf16 v[90:93], v[6:9], v[82:85], 0
	v_mfma_f32_16x16x32_bf16 v[94:97], v[34:37], v[82:85], 0
	v_mfma_f32_16x16x32_bf16 v[82:85], v[38:41], v[82:85], 0
	s_waitcnt lgkmcnt(0)
	v_mfma_f32_16x16x32_bf16 v[86:89], v[10:13], v[178:181], v[86:89]
	v_mfma_f32_16x16x32_bf16 v[90:93], v[14:17], v[178:181], v[90:93]
	v_mfma_f32_16x16x32_bf16 v[94:97], v[42:45], v[178:181], v[94:97]
	v_mfma_f32_16x16x32_bf16 v[82:85], v[46:49], v[178:181], v[82:85]
	ds_read_b128 v[178:181], v161 offset:128
	s_waitcnt lgkmcnt(0)
	v_mfma_f32_16x16x32_bf16 v[86:89], v[18:21], v[178:181], v[86:89]
	v_mfma_f32_16x16x32_bf16 v[90:93], v[22:25], v[178:181], v[90:93]
	v_mfma_f32_16x16x32_bf16 v[182:185], v[50:53], v[178:181], v[94:97]
	v_mfma_f32_16x16x32_bf16 v[82:85], v[54:57], v[178:181], v[82:85]
	ds_read_b128 v[178:181], v161 offset:192
	s_waitcnt lgkmcnt(0)
	v_mfma_f32_16x16x32_bf16 v[186:189], v[26:29], v[178:181], v[86:89]
	v_mfma_f32_16x16x32_bf16 v[94:97], v[30:33], v[178:181], v[90:93]
	s_nop 6
	v_add_f32_e32 v124, v66, v186
	v_mul_f32_e32 v124, 0xbfb8aa3b, v124
	v_exp_f32_e32 v124, v124
	v_mfma_f32_16x16x32_bf16 v[86:89], v[58:61], v[178:181], v[182:185]
	ds_read_b128 v[90:93], v152 offset:17408
	v_add_f32_e32 v94, v70, v94
	v_add_f32_e32 v96, v72, v96
	v_mfma_f32_16x16x32_bf16 v[82:85], v[62:65], v[178:181], v[82:85]
	v_add_f32_e32 v180, v68, v188
	v_mul_f32_e32 v180, 0xbfb8aa3b, v180
	v_exp_f32_e32 v180, v180
	v_mul_f32_e32 v94, 0xbfb8aa3b, v94
	v_mul_f32_e32 v96, 0xbfb8aa3b, v96
	v_add_f32_e32 v124, 1.0, v124
	v_exp_f32_e32 v94, v94
	v_add_f32_e32 v180, 1.0, v180
	v_exp_f32_e32 v96, v96
	v_rcp_f32_e32 v125, v124
	v_rcp_f32_e32 v181, v180
	v_add_f32_e32 v94, 1.0, v94
	v_add_f32_e32 v96, 1.0, v96
	v_rcp_f32_e32 v124, v94
	v_mul_f32_e32 v94, v139, v125
	v_rcp_f32_e32 v180, v96
	v_mul_f32_e32 v96, v141, v181
	v_mul_f32_e32 v94, 0x3fb8aa3b, v94
	v_mul_f32_e32 v96, 0x3fb8aa3b, v96
	v_exp_f32_e32 v94, v94
	v_exp_f32_e32 v96, v96
	v_add_f32_e32 v95, v71, v95
	v_add_f32_e32 v97, v73, v97
	v_fma_f32 v125, -v94, v94, 1.0
	v_fma_f32 v181, -v96, v96, 1.0
	v_max_f32_e32 v125, 0, v125
	v_max_f32_e32 v181, 0, v181
	v_sqrt_f32_e32 v178, v125
	v_add_f32_e32 v125, v67, v187
	v_sqrt_f32_e32 v182, v181
	v_add_f32_e32 v181, v69, v189
	v_mul_f32_e32 v125, 0xbfb8aa3b, v125
	v_mul_f32_e32 v181, 0xbfb8aa3b, v181
	v_exp_f32_e32 v125, v125
	v_exp_f32_e32 v181, v181
	v_mul_f32_e32 v95, 0xbfb8aa3b, v95
	v_mul_f32_e32 v97, 0xbfb8aa3b, v97
	v_add_f32_e32 v125, 1.0, v125
	v_exp_f32_e32 v95, v95
	v_add_f32_e32 v181, 1.0, v181
	v_exp_f32_e32 v97, v97
	v_rcp_f32_e32 v179, v125
	v_rcp_f32_e32 v183, v181
	v_add_f32_e32 v95, 1.0, v95
	v_add_f32_e32 v97, 1.0, v97
	v_rcp_f32_e32 v125, v95
	v_mul_f32_e32 v95, v140, v179
	v_rcp_f32_e32 v181, v97
	v_mul_f32_e32 v97, v142, v183
	v_mul_f32_e32 v95, 0x3fb8aa3b, v95
	v_mul_f32_e32 v97, 0x3fb8aa3b, v97
	v_exp_f32_e32 v95, v95
	v_exp_f32_e32 v97, v97
	v_add_f32_e32 v86, v74, v86
	v_add_f32_e32 v87, v75, v87
	v_add_f32_e32 v88, v76, v88
	v_add_f32_e32 v89, v77, v89
	v_fma_f32 v179, -v95, v95, 1.0
	v_fma_f32 v183, -v97, v97, 1.0
	v_mul_f32_e32 v86, 0xbfb8aa3b, v86
	v_mul_f32_e32 v87, 0xbfb8aa3b, v87
	v_mul_f32_e32 v88, 0xbfb8aa3b, v88
	v_mul_f32_e32 v89, 0xbfb8aa3b, v89
	v_max_f32_e32 v179, 0, v179
	v_max_f32_e32 v183, 0, v183
	v_exp_f32_e32 v86, v86
	v_exp_f32_e32 v87, v87
	v_exp_f32_e32 v88, v88
	v_exp_f32_e32 v89, v89
	v_sqrt_f32_e32 v179, v179
	v_sqrt_f32_e32 v183, v183
	v_add_f32_e32 v82, v78, v82
	v_add_f32_e32 v83, v79, v83
	v_add_f32_e32 v84, v80, v84
	v_add_f32_e32 v85, v81, v85
	v_mul_f32_e32 v82, 0xbfb8aa3b, v82
	v_mul_f32_e32 v83, 0xbfb8aa3b, v83
	v_mul_f32_e32 v84, 0xbfb8aa3b, v84
	v_mul_f32_e32 v85, 0xbfb8aa3b, v85
	s_waitcnt lgkmcnt(0)
	v_pk_mul_f32 v[90:91], v[90:91], v[124:125]
	v_pk_mul_f32 v[92:93], v[92:93], v[180:181]
	v_add_f32_e32 v86, 1.0, v86
	v_exp_f32_e32 v82, v82
	v_add_f32_e32 v87, 1.0, v87
	v_exp_f32_e32 v83, v83
	v_add_f32_e32 v88, 1.0, v88
	v_exp_f32_e32 v84, v84
	v_add_f32_e32 v89, 1.0, v89
	v_exp_f32_e32 v85, v85
	v_pk_mul_f32 v[92:93], v[92:93], v[182:183]
	v_pk_mul_f32 v[90:91], v[90:91], v[178:179]
	ds_write_b128 v153, v[94:97] offset:33792
	ds_write_b128 v153, v[90:93] offset:51200
	v_rcp_f32_e32 v94, v86
	v_rcp_f32_e32 v95, v87
	v_rcp_f32_e32 v96, v88
	v_rcp_f32_e32 v97, v89
	v_add_f32_e32 v82, 1.0, v82
	v_add_f32_e32 v83, 1.0, v83
	v_add_f32_e32 v84, 1.0, v84
	v_add_f32_e32 v85, 1.0, v85
	v_rcp_f32_e32 v86, v82
	v_mul_f32_e32 v82, v143, v94
	v_rcp_f32_e32 v87, v83
	v_mul_f32_e32 v83, v144, v95
	v_rcp_f32_e32 v88, v84
	v_mul_f32_e32 v84, v145, v96
	v_rcp_f32_e32 v89, v85
	v_mul_f32_e32 v85, v107, v97
	v_mul_f32_e32 v82, 0x3fb8aa3b, v82
	v_mul_f32_e32 v83, 0x3fb8aa3b, v83
	v_mul_f32_e32 v84, 0x3fb8aa3b, v84
	v_mul_f32_e32 v85, 0x3fb8aa3b, v85
	v_exp_f32_e32 v82, v82
	v_exp_f32_e32 v83, v83
	v_exp_f32_e32 v84, v84
	v_exp_f32_e32 v85, v85
	ds_read_b128 v[90:93], v152 offset:17472
	v_fma_f32 v94, -v82, v82, 1.0
	v_fma_f32 v95, -v83, v83, 1.0
	v_fma_f32 v96, -v84, v84, 1.0
	v_fma_f32 v97, -v85, v85, 1.0
	v_max_f32_e32 v94, 0, v94
	v_max_f32_e32 v95, 0, v95
	v_max_f32_e32 v96, 0, v96
	v_max_f32_e32 v97, 0, v97
	v_sqrt_f32_e32 v94, v94
	v_sqrt_f32_e32 v95, v95
	v_sqrt_f32_e32 v96, v96
	v_sqrt_f32_e32 v97, v97
	s_waitcnt lgkmcnt(0)
	v_pk_mul_f32 v[86:87], v[90:91], v[86:87]
	v_pk_mul_f32 v[88:89], v[92:93], v[88:89]
	v_pk_mul_f32 v[86:87], v[86:87], v[94:95]
	v_pk_mul_f32 v[88:89], v[88:89], v[96:97]
	ds_write_b128 v153, v[82:85] offset:33856
	ds_write_b128 v153, v[86:89] offset:51264
	s_waitcnt lgkmcnt(0)
	s_barrier
; __device__ __forceinline__ float bf2f(bf16 b) { return __uint_as_float(((unsigned)b) << 16); }
; __device__ __forceinline__ unsigned cvtpk(float lo, float hi) { const f32x2 v = {lo, hi}; return __builtin_bit_cast(unsigned, __builtin_convertvector(v, bf16x2_t)); }
; __device__ __forceinline__ void unit(LAS unsigned char* lds, const bf16* __restrict__ xr, const bf16* __restrict__ yg, const float* __restrict__ conv_w, const float* __restrict__ conv_b, const bf16* __restrict__ wga_t, const bf16* __restrict__ wgx_t, ...
;     ...
;         { float A = 1.f, B = 0.f;
; #pragma unroll
;             for (int i = 0; i < 8; ++i) { a8[i] = SA[(8 * sg + i) * 68 + cc]; b8[i] = SB[(8 * sg + i) * 68 + cc]; B = a8[i] * B + b8[i]; A *= a8[i]; }
;             SC[sg * 64 + cc] = (f32x2){A, B}; }
;         asm volatile("s_waitcnt lgkmcnt(0)" ::: "memory"); __builtin_amdgcn_s_barrier(); asm volatile("" ::: "memory");
;         {
;             float hcur = HS[cc];
; #pragma unroll
;             for (int s2 = 0; s2 < 7; ++s2) { const f32x2 ab = SC[s2 * 64 + cc]; if (s2 < sg) hcur = ab.x * hcur + ab.y; }
;             float ysq[8];
; #pragma unroll
;             for (int i = 0; i < 8; ++i) { hcur = a8[i] * hcur + b8[i]; const float x = bf2f(ycur[i]);
;                 const float u2 = 1.5957691216f * (x + 0.044715f * x * x * x);
;                 const float y = hcur * (x * __builtin_amdgcn_rcpf(1.0f + __builtin_amdgcn_exp2f(-LOG2E * u2))); outp[((size_t)t0 + i) * DM] = (bf16)(cvtpk(y, 0.f) & 0xffffu); ysq[i] = y * y; }
	v_add_u32_e32 v82, 0x8400, v156
	v_add_u32_e32 v83, 0xc800, v156
	ds_read2_b32 v[124:125], v82 offset1:68
	ds_read2_b32 v[96:97], v83 offset1:68
	ds_read2_b32 v[94:95], v82 offset0:136 offset1:204
	ds_read2_b32 v[92:93], v83 offset0:136 offset1:204
	v_add_u32_e32 v83, 0x8800, v156
	v_add_u32_e32 v178, 0xcc00, v156
	ds_read2_b32 v[88:89], v83 offset0:16 offset1:84
	ds_read2_b32 v[86:87], v178 offset0:16 offset1:84
	s_waitcnt lgkmcnt(4)
	v_fma_f32 v84, 0, v124, v96
	v_fma_f32 v84, v84, v125, v97
	s_waitcnt lgkmcnt(2)
	v_fma_f32 v82, v84, v94, v92
	v_fma_f32 v82, v82, v95, v93
	s_waitcnt lgkmcnt(0)
	v_fma_f32 v91, v82, v88, v86
	ds_read2_b32 v[84:85], v83 offset0:152 offset1:220
	ds_read2_b32 v[82:83], v178 offset0:152 offset1:220
	v_mul_f32_e32 v90, v124, v125
	v_mov_b32_e32 v178, v94
	v_mov_b32_e32 v179, v89
	v_mov_b32_e32 v180, v95
	v_mov_b32_e32 v181, v87
	v_mul_f32_e32 v182, v90, v94
	v_pk_fma_f32 v[90:91], v[90:91], v[178:179], v[180:181]
	v_mul_f32_e32 v182, v182, v95
	v_mov_b32_e32 v183, v91
	v_mov_b32_e32 v90, v88
	s_waitcnt lgkmcnt(1)
	v_mov_b32_e32 v91, v84
	v_pk_mul_f32 v[178:179], v[182:183], v[90:91]
	v_mov_b32_e32 v180, v89
	v_mov_b32_e32 v184, v89
	s_waitcnt lgkmcnt(0)
	v_mov_b32_e32 v185, v82
	v_pk_mul_f32 v[178:179], v[178:179], v[180:181]
	v_pk_fma_f32 v[90:91], v[182:183], v[90:91], v[184:185]
	v_mov_b32_e32 v180, v85
	v_mov_b32_e32 v90, v178
	v_pk_mul_f32 v[178:179], v[178:179], v[84:85]
	v_mov_b32_e32 v182, v85
	v_mov_b32_e32 v183, v83
	v_pk_mul_f32 v[178:179], v[178:179], v[180:181]
	v_pk_fma_f32 v[90:91], v[90:91], v[84:85], v[182:183]
	s_nop 0
	v_mov_b32_e32 v179, v91
	ds_write_b64 v149, v[178:179]
	s_waitcnt lgkmcnt(0)
	s_barrier
	ds_read_b32 v90, v131
	ds_read_b64 v[214:215], v129
	ds_read_b64 v[216:217], v129 offset:512
	ds_read_b64 v[218:219], v129 offset:1024
	ds_read_b64 v[220:221], v129 offset:1536
	ds_read_b64 v[222:223], v129 offset:2048
	ds_read_b64 v[224:225], v129 offset:2560
	ds_read_b64 v[226:227], v129 offset:3072
	s_waitcnt lgkmcnt(6)
	v_fmac_f32_e32 v215, v90, v214
	v_cndmask_b32_e64 v90, v215, v90, s[4:5]
	s_waitcnt lgkmcnt(5)
	v_fmac_f32_e32 v217, v90, v216
	v_cndmask_b32_e64 v90, v90, v217, s[50:51]
	s_waitcnt lgkmcnt(4)
	v_fmac_f32_e32 v219, v90, v218
	v_cndmask_b32_e64 v90, v90, v219, s[54:55]
	s_waitcnt lgkmcnt(3)
	v_fmac_f32_e32 v221, v90, v220
	v_cndmask_b32_e64 v90, v90, v221, s[60:61]
	s_waitcnt lgkmcnt(2)
	v_fmac_f32_e32 v223, v90, v222
	v_cndmask_b32_e64 v90, v90, v223, s[62:63]
	s_waitcnt lgkmcnt(1)
	v_fmac_f32_e32 v225, v90, v224
	v_cndmask_b32_e64 v90, v90, v225, s[64:65]
	s_waitcnt lgkmcnt(0)
	v_fmac_f32_e32 v227, v90, v226
	v_cndmask_b32_e64 v90, v90, v227, s[66:67]
	s_waitcnt lgkmcnt(0)
	v_fma_f32 v96, v124, v90, v96
	v_lshlrev_b32_e32 v90, 16, v177
	v_mul_f32_e32 v91, 0x3d372713, v90
	v_mul_f32_e32 v91, v91, v90
	v_fma_f32 v91, v91, v90, v90
	v_mul_f32_e32 v91, 0x3fcc422a, v91
	v_mul_f32_e32 v91, 0xbfb8aa3b, v91
	v_exp_f32_e32 v91, v91
	v_fmac_f32_e32 v97, v125, v96
	s_mov_b32 s70, 0x9c001000
	v_fma_f32 v92, v94, v97, v92
	v_add_f32_e32 v91, 1.0, v91
	v_rcp_f32_e32 v91, v91
	v_lshlrev_b32_e32 v94, 16, v171
	v_fmac_f32_e32 v93, v95, v92
	v_fma_f32 v86, v88, v93, v86
	v_mul_f32_e32 v90, v91, v90
	v_mul_f32_e32 v177, v90, v96
	v_lshl_add_u64 v[90:91], s[22:23], 0, v[122:123]
	v_add_co_u32_e32 v178, vcc, 0x9c000000, v90
	v_cvt_pk_bf16_f32 v124, v177, s0
	s_nop 0
	v_addc_co_u32_e32 v179, vcc, 0, v91, vcc
	v_lshlrev_b32_e32 v96, 16, v176
	global_store_short v[178:179], v124, off offset:2048
	v_mul_f32_e32 v124, 0x3d372713, v96
	v_mul_f32_e32 v124, v124, v96
	v_fma_f32 v124, v124, v96, v96
	v_mul_f32_e32 v124, 0x3fcc422a, v124
	v_mul_f32_e32 v124, 0xbfb8aa3b, v124
	v_exp_f32_e32 v124, v124
	v_lshlrev_b32_e32 v88, 16, v165
	v_fmac_f32_e32 v87, v89, v86
	v_fma_f32 v82, v84, v87, v82
	v_add_f32_e32 v124, 1.0, v124
	v_rcp_f32_e32 v124, v124
	v_lshlrev_b32_e32 v84, 16, v163
	v_fmac_f32_e32 v83, v85, v82
	v_mul_f32_e32 v178, v177, v177
	v_mul_f32_e32 v96, v124, v96
	v_mul_f32_e32 v176, v96, v97
	v_add_co_u32_e32 v124, vcc, s70, v90
	v_cvt_pk_bf16_f32 v96, v176, s0
	s_nop 0
	v_addc_co_u32_e32 v125, vcc, 0, v91, vcc
	global_store_short v[124:125], v96, off offset:2048
	v_mul_f32_e32 v96, 0x3d372713, v94
	v_mul_f32_e32 v96, v96, v94
	v_fma_f32 v96, v96, v94, v94
	v_mul_f32_e32 v96, 0x3fcc422a, v96
	v_mul_f32_e32 v96, 0xbfb8aa3b, v96
	v_exp_f32_e32 v96, v96
	s_mov_b32 s70, 0x9c002000
	v_mul_f32_e32 v124, v176, v176
	v_add_f32_e32 v96, 1.0, v96
	v_rcp_f32_e32 v96, v96
	s_nop 0
	v_mul_f32_e32 v94, v96, v94
	v_mul_f32_e32 v125, v94, v92
	v_add_co_u32_e32 v96, vcc, s70, v90
	v_cvt_pk_bf16_f32 v94, v125, s0
	s_nop 0
	v_addc_co_u32_e32 v97, vcc, 0, v91, vcc
	v_lshlrev_b32_e32 v92, 16, v166
	global_store_short v[96:97], v94, off offset:2048
	v_mul_f32_e32 v94, 0x3d372713, v92
	v_mul_f32_e32 v94, v94, v92
	v_fma_f32 v94, v94, v92, v92
	v_mul_f32_e32 v94, 0x3fcc422a, v94
	v_mul_f32_e32 v94, 0xbfb8aa3b, v94
	v_exp_f32_e32 v94, v94
	s_mov_b32 s70, 0x9c003000
	v_mul_f32_e32 v96, v125, v125
	v_add_f32_e32 v94, 1.0, v94
	v_rcp_f32_e32 v94, v94
	s_nop 0
	v_mul_f32_e32 v92, v94, v92
	v_mul_f32_e32 v97, v92, v93
	v_add_co_u32_e32 v94, vcc, s70, v90
	v_cvt_pk_bf16_f32 v92, v97, s0
	s_nop 0
	v_addc_co_u32_e32 v95, vcc, 0, v91, vcc
	global_store_short v[94:95], v92, off offset:2048
	v_mul_f32_e32 v92, 0x3d372713, v88
	v_mul_f32_e32 v92, v92, v88
	v_fma_f32 v92, v92, v88, v88
	v_mul_f32_e32 v92, 0x3fcc422a, v92
	v_mul_f32_e32 v92, 0xbfb8aa3b, v92
	v_exp_f32_e32 v92, v92
	s_mov_b32 s70, 0x9c004000
	v_mul_f32_e32 v94, v97, v97
	v_add_f32_e32 v92, 1.0, v92
	v_rcp_f32_e32 v92, v92
	s_nop 0
	v_mul_f32_e32 v88, v92, v88
; __device__ __forceinline__ float bf2f(bf16 b) { return __uint_as_float(((unsigned)b) << 16); }
; __device__ __forceinline__ unsigned cvtpk(float lo, float hi) { const f32x2 v = {lo, hi}; return __builtin_bit_cast(unsigned, __builtin_convertvector(v, bf16x2_t)); }
; __device__ __forceinline__ void unit(LAS unsigned char* lds, const bf16* __restrict__ xr, const bf16* __restrict__ yg, const float* __restrict__ conv_w, const float* __restrict__ conv_b, const bf16* __restrict__ wga_t, const bf16* __restrict__ wgx_t, ...
;     ...
;             for (int i = 0; i < 8; ++i) { hcur = a8[i] * hcur + b8[i]; const float x = bf2f(ycur[i]);
;                 const float u2 = 1.5957691216f * (x + 0.044715f * x * x * x);
;                 const float y = hcur * (x * __builtin_amdgcn_rcpf(1.0f + __builtin_amdgcn_exp2f(-LOG2E * u2))); outp[((size_t)t0 + i) * DM] = (bf16)(cvtpk(y, 0.f) & 0xffffu); ysq[i] = y * y; }
; #pragma unroll
;             for (int i = 0; i < 8; ++i) { float v = ysq[i];
;                 v += __builtin_bit_cast(float, __builtin_amdgcn_update_dpp(0, __builtin_bit_cast(int, v), 0xB1, 0xf, 0xf, true));
;                 v += __builtin_bit_cast(float, __builtin_amdgcn_update_dpp(0, __builtin_bit_cast(int, v), 0x4E, 0xf, 0xf, true));
;                 v += __builtin_bit_cast(float, __builtin_amdgcn_update_dpp(0, __builtin_bit_cast(int, v), 0x141, 0xf, 0xf, true));
;                 v += __builtin_bit_cast(float, __builtin_amdgcn_update_dpp(0, __builtin_bit_cast(int, v), 0x140, 0xf, 0xf, true));
;                 v += __builtin_bit_cast(float, __builtin_amdgcn_update_dpp(0, __builtin_bit_cast(int, v), 0x142, 0xa, 0xf, false));
;                 v += __builtin_bit_cast(float, __builtin_amdgcn_update_dpp(0, __builtin_bit_cast(int, v), 0x143, 0xc, 0xf, false));
;                 ysq[i] = v; }
	v_mul_f32_e32 v95, v88, v86
	v_add_co_u32_e32 v92, vcc, s70, v90
	v_cvt_pk_bf16_f32 v88, v95, s0
	s_nop 0
	v_addc_co_u32_e32 v93, vcc, 0, v91, vcc
	v_lshlrev_b32_e32 v86, 16, v164
	global_store_short v[92:93], v88, off offset:2048
	v_mul_f32_e32 v88, 0x3d372713, v86
	v_mul_f32_e32 v88, v88, v86
	v_fma_f32 v88, v88, v86, v86
	v_mul_f32_e32 v88, 0x3fcc422a, v88
	v_mul_f32_e32 v88, 0xbfb8aa3b, v88
	v_exp_f32_e32 v88, v88
	s_mov_b32 s70, 0x9c005000
	v_mul_f32_e32 v92, v95, v95
	v_add_f32_e32 v88, 1.0, v88
	v_rcp_f32_e32 v88, v88
	s_nop 0
	v_mul_f32_e32 v86, v88, v86
	v_mul_f32_e32 v93, v86, v87
	v_add_co_u32_e32 v88, vcc, s70, v90
	v_cvt_pk_bf16_f32 v86, v93, s0
	s_nop 0
	v_addc_co_u32_e32 v89, vcc, 0, v91, vcc
	global_store_short v[88:89], v86, off offset:2048
	v_mul_f32_e32 v86, 0x3d372713, v84
	v_mul_f32_e32 v86, v86, v84
	v_fma_f32 v86, v86, v84, v84
	v_mul_f32_e32 v86, 0x3fcc422a, v86
	v_mul_f32_e32 v86, 0xbfb8aa3b, v86
	v_exp_f32_e32 v86, v86
	s_mov_b32 s70, 0x9c006000
	v_mul_f32_e32 v164, v93, v93
	v_mov_b32_dpp v89, v94 quad_perm:[1,0,3,2] row_mask:0xf bank_mask:0xf bound_ctrl:1
	v_add_f32_e32 v86, 1.0, v86
	v_rcp_f32_e32 v86, v86
	v_fmac_f32_e32 v89, v97, v97
	v_mov_b32_dpp v94, v164 quad_perm:[1,0,3,2] row_mask:0xf bank_mask:0xf bound_ctrl:1
	v_fmac_f32_e32 v94, v93, v93
	v_mul_f32_e32 v84, v86, v84
	v_mul_f32_e32 v163, v84, v82
	v_add_co_u32_e32 v86, vcc, s70, v90
	v_cvt_pk_bf16_f32 v84, v163, s0
	s_nop 0
	v_addc_co_u32_e32 v87, vcc, 0, v91, vcc
	v_lshlrev_b32_e32 v82, 16, v162
	global_store_short v[86:87], v84, off offset:2048
	v_mul_f32_e32 v84, 0x3d372713, v82
	v_mul_f32_e32 v84, v84, v82
	v_fma_f32 v84, v84, v82, v82
	v_mul_f32_e32 v84, 0x3fcc422a, v84
	v_mul_f32_e32 v84, 0xbfb8aa3b, v84
	v_exp_f32_e32 v84, v84
	s_mov_b32 s70, 0x9c007000
	v_mul_f32_e32 v165, v163, v163
	v_mov_b32_dpp v87, v96 quad_perm:[1,0,3,2] row_mask:0xf bank_mask:0xf bound_ctrl:1
	v_add_f32_e32 v84, 1.0, v84
	v_rcp_f32_e32 v84, v84
	v_fmac_f32_e32 v87, v125, v125
	v_add_f32_dpp v89, v89, v89 quad_perm:[2,3,0,1] row_mask:0xf bank_mask:0xf bound_ctrl:1
	v_add_f32_dpp v93, v94, v94 quad_perm:[2,3,0,1] row_mask:0xf bank_mask:0xf bound_ctrl:1
	v_mul_f32_e32 v82, v84, v82
	v_mul_f32_e32 v162, v82, v83
	v_add_co_u32_e32 v84, vcc, s70, v90
	v_cvt_pk_bf16_f32 v82, v162, s0
	s_nop 0
	v_addc_co_u32_e32 v85, vcc, 0, v91, vcc
	v_mul_f32_e32 v166, v162, v162
	v_mov_b32_dpp v91, v92 quad_perm:[1,0,3,2] row_mask:0xf bank_mask:0xf bound_ctrl:1
	global_store_short v[84:85], v82, off offset:2048
	v_mov_b32_dpp v82, v178 quad_perm:[1,0,3,2] row_mask:0xf bank_mask:0xf bound_ctrl:1
	v_mov_b32_dpp v85, v124 quad_perm:[1,0,3,2] row_mask:0xf bank_mask:0xf bound_ctrl:1
	v_fmac_f32_e32 v91, v95, v95
	v_mov_b32_dpp v95, v165 quad_perm:[1,0,3,2] row_mask:0xf bank_mask:0xf bound_ctrl:1
	v_mov_b32_dpp v97, v166 quad_perm:[1,0,3,2] row_mask:0xf bank_mask:0xf bound_ctrl:1
	v_fmac_f32_e32 v82, v177, v177
	v_fmac_f32_e32 v85, v176, v176
	v_fmac_f32_e32 v95, v163, v163
	v_fmac_f32_e32 v97, v162, v162
	v_add_f32_dpp v82, v82, v82 quad_perm:[2,3,0,1] row_mask:0xf bank_mask:0xf bound_ctrl:1
	v_add_f32_dpp v85, v85, v85 quad_perm:[2,3,0,1] row_mask:0xf bank_mask:0xf bound_ctrl:1
	v_add_f32_dpp v87, v87, v87 quad_perm:[2,3,0,1] row_mask:0xf bank_mask:0xf bound_ctrl:1
	v_add_f32_dpp v91, v91, v91 quad_perm:[2,3,0,1] row_mask:0xf bank_mask:0xf bound_ctrl:1
	v_add_f32_dpp v95, v95, v95 quad_perm:[2,3,0,1] row_mask:0xf bank_mask:0xf bound_ctrl:1
	v_add_f32_dpp v97, v97, v97 quad_perm:[2,3,0,1] row_mask:0xf bank_mask:0xf bound_ctrl:1
	v_add_f32_dpp v82, v82, v82 row_half_mirror row_mask:0xf bank_mask:0xf bound_ctrl:1
	v_add_f32_dpp v85, v85, v85 row_half_mirror row_mask:0xf bank_mask:0xf bound_ctrl:1
	v_add_f32_dpp v87, v87, v87 row_half_mirror row_mask:0xf bank_mask:0xf bound_ctrl:1
	v_add_f32_dpp v89, v89, v89 row_half_mirror row_mask:0xf bank_mask:0xf bound_ctrl:1
	v_add_f32_dpp v91, v91, v91 row_half_mirror row_mask:0xf bank_mask:0xf bound_ctrl:1
	v_add_f32_dpp v93, v93, v93 row_half_mirror row_mask:0xf bank_mask:0xf bound_ctrl:1
	v_add_f32_dpp v95, v95, v95 row_half_mirror row_mask:0xf bank_mask:0xf bound_ctrl:1
	v_add_f32_dpp v97, v97, v97 row_half_mirror row_mask:0xf bank_mask:0xf bound_ctrl:1
	v_add_f32_dpp v82, v82, v82 row_mirror row_mask:0xf bank_mask:0xf bound_ctrl:1
	v_mov_b32_e32 v84, 0
	v_add_f32_dpp v85, v85, v85 row_mirror row_mask:0xf bank_mask:0xf bound_ctrl:1
	v_mov_b32_e32 v86, 0
	v_add_f32_dpp v87, v87, v87 row_mirror row_mask:0xf bank_mask:0xf bound_ctrl:1
	v_mov_b32_e32 v88, 0
	v_add_f32_dpp v89, v89, v89 row_mirror row_mask:0xf bank_mask:0xf bound_ctrl:1
	v_mov_b32_e32 v90, 0
	v_add_f32_dpp v91, v91, v91 row_mirror row_mask:0xf bank_mask:0xf bound_ctrl:1
	v_mov_b32_e32 v92, 0
	v_add_f32_dpp v93, v93, v93 row_mirror row_mask:0xf bank_mask:0xf bound_ctrl:1
	v_mov_b32_e32 v94, 0
	v_add_f32_dpp v95, v95, v95 row_mirror row_mask:0xf bank_mask:0xf bound_ctrl:1
	v_mov_b32_e32 v96, 0
	v_add_f32_dpp v97, v97, v97 row_mirror row_mask:0xf bank_mask:0xf bound_ctrl:1
	v_mov_b32_e32 v124, 0
	v_mov_b32_dpp v84, v82 row_bcast:15 row_mask:0xa bank_mask:0xf
	v_mov_b32_dpp v86, v85 row_bcast:15 row_mask:0xa bank_mask:0xf
	v_mov_b32_dpp v88, v87 row_bcast:15 row_mask:0xa bank_mask:0xf
	v_mov_b32_dpp v90, v89 row_bcast:15 row_mask:0xa bank_mask:0xf
	v_mov_b32_dpp v92, v91 row_bcast:15 row_mask:0xa bank_mask:0xf
	v_mov_b32_dpp v94, v93 row_bcast:15 row_mask:0xa bank_mask:0xf
	v_mov_b32_dpp v96, v95 row_bcast:15 row_mask:0xa bank_mask:0xf
	v_mov_b32_dpp v124, v97 row_bcast:15 row_mask:0xa bank_mask:0xf
	v_add_f32_e32 v82, v82, v84
	v_mov_b32_e32 v84, 0
	v_add_f32_e32 v85, v85, v86
	v_mov_b32_e32 v86, 0
	v_add_f32_e32 v87, v87, v88
	v_mov_b32_e32 v88, 0
	v_add_f32_e32 v89, v89, v90
	v_mov_b32_e32 v90, 0
	v_add_f32_e32 v91, v91, v92
	v_mov_b32_e32 v92, 0
	v_add_f32_e32 v93, v93, v94
	v_mov_b32_e32 v94, 0
	v_add_f32_e32 v95, v95, v96
	v_mov_b32_e32 v96, 0
	v_add_f32_e32 v97, v97, v124
	v_mov_b32_e32 v124, 0
	v_mov_b32_dpp v84, v82 row_bcast:31 row_mask:0xc bank_mask:0xf
	v_mov_b32_dpp v86, v85 row_bcast:31 row_mask:0xc bank_mask:0xf
	v_mov_b32_dpp v88, v87 row_bcast:31 row_mask:0xc bank_mask:0xf
	v_mov_b32_dpp v90, v89 row_bcast:31 row_mask:0xc bank_mask:0xf
	v_mov_b32_dpp v92, v91 row_bcast:31 row_mask:0xc bank_mask:0xf
	v_mov_b32_dpp v94, v93 row_bcast:31 row_mask:0xc bank_mask:0xf
	v_mov_b32_dpp v96, v95 row_bcast:31 row_mask:0xc bank_mask:0xf
	v_mov_b32_dpp v124, v97 row_bcast:31 row_mask:0xc bank_mask:0xf
	s_and_saveexec_b64 s[70:71], s[8:9]
	s_cbranch_execz .LBB5_965
; __device__ __forceinline__ void unit(LAS unsigned char* lds, const bf16* __restrict__ xr, const bf16* __restrict__ yg, const float* __restrict__ conv_w, const float* __restrict__ conv_b, const bf16* __restrict__ wga_t, const bf16* __restrict__ wgx_t, ...
;     ...
;             if (lane == 63) {
; #pragma unroll
;                 for (int i = 0; i < 8; ++i) ssl[((size_t)b * SEQ + t0 + 8 * sg + i) * 16 + g] = ysq[i]; }
;             asm volatile("s_waitcnt lgkmcnt(0)" ::: "memory"); __builtin_amdgcn_s_barrier(); asm volatile("" ::: "memory");
;             if (sg == 7) HS[cc] = hcur;
	s_add_u32 s92, s22, s34
	v_add_f32_e32 v82, v82, v84
	s_addc_u32 s93, s23, s89
	v_add_f32_e32 v97, v97, v124
	v_add_f32_e32 v95, v95, v96
	v_add_f32_e32 v93, v93, v94
	v_add_f32_e32 v91, v91, v92
	v_add_f32_e32 v89, v89, v90
	v_add_f32_e32 v87, v87, v88
	v_add_f32_e32 v85, v85, v86
	global_store_dword v99, v82, s[92:93] offset:-256
	global_store_dword v99, v85, s[92:93] offset:-192
	global_store_dword v99, v87, s[92:93] offset:-128
	global_store_dword v99, v89, s[92:93] offset:-64
	global_store_dword v99, v91, s[92:93]
	global_store_dword v99, v93, s[92:93] offset:64
	global_store_dword v99, v95, s[92:93] offset:128
	global_store_dword v99, v97, s[92:93] offset:192
.LBB5_965:
	s_or_b64 exec, exec, s[70:71]
	s_waitcnt lgkmcnt(0)
	s_barrier
	s_andn2_b64 vcc, exec, s[42:43]
	s_cbranch_vccnz .LBB5_936
	ds_write_b32 v131, v83
	s_branch .LBB5_936
.LBB5_973:
	v_add_co_u32_e32 v92, vcc, 0xfffff000, v90
	s_nop 1
	v_addc_co_u32_e32 v93, vcc, -1, v91, vcc
	global_load_dword v137, v[92:93], off offset:-2048
	v_cndmask_b32_e64 v92, 0, 1, s[42:43]
	v_cmp_ne_u32_e64 s[4:5], 1, v92
	s_andn2_b64 vcc, exec, s[42:43]
	s_cbranch_vccnz .LBB5_933
